# attention-phase copy batches rounded up to an even item count (4 + 2 instead of 3 + 3) so both copy buffers stay in use
# baseline (speedup 1.0000x reference)
; __device__ __forceinline__ void convert_range(const float* w_gate, const float* w_up, const float* w_down, bf16* BTGU, bf16* BTD, int x0, int x1, LAS unsigned char* scr, int lane) {
;     ...
;     for (int x = x0; x < x1; x += 2) {
;         const bool hasB = x + 1 < x1;
;         if (hasB) { B = xitem(w_gate, w_up, w_down, BTGU, BTD, x + 1); t64_load(B.src, B.ldw, lane, tc); }
;         t64_finish(ta, A.dst, A.ldd, A.f8, scr, lane);
;         if (hasB) {
;             if (x + 2 < x1) { A = xitem(w_gate, w_up, w_down, BTGU, BTD, x + 2); t64_load(A.src, A.ldw, lane, ta); }
;             t64_finish(tc, B.dst, B.ldd, B.f8, scr, lane);
;         }
;     }
; __global__ void __launch_bounds__(512, 2) hymba_fwd(Args args) {
;     ...
;             constexpr int CV_LO = CV_N1, CV_HI = CV_GU + CV_D - CV_N5, CV_EXP = CV_HI - CV_LO;
;             const int nA = (512 - bx + G - 1) / G;
;             const int per_wave = (CV_EXP + NGW - 1) / NGW;
;             const int c_lo = CV_LO + gw * per_wave, c_hi = (c_lo + per_wave < CV_HI) ? c_lo + per_wave : CV_HI;
;             const int nsteps = nA > 0 ? nA : 1, per_batch = (per_wave + nsteps - 1) / nsteps;
;             int ia = 0, ic = c_lo;
; #pragma unroll 1
;             for (int hs = 0; hs < 2 * nsteps; ++hs) {
;                 const bool doA = (((hs & 1) == 0) == (wave < 4));
.LBB0_212:
	s_or_b64 exec, exec, s[0:1]
	s_abs_i32 s0, s3
	v_cvt_f32_u32_e32 v1, s0
	s_mul_i32 s1, s92, 0x3000
	s_add_i32 s68, s1, 0
	s_sub_i32 s1, s3, s2
	v_rcp_iflag_f32_e32 v1, v1
	s_add_i32 s6, s1, 0x1ff
	s_sub_i32 s1, 0xfffffe01, s1
	s_xor_b32 s7, s6, s3
	v_mul_f32_e32 v1, 0x4f7ffffe, v1
	v_cvt_u32_f32_e32 v1, v1
	s_max_i32 s1, s6, s1
	s_sub_i32 s6, 0, s0
	s_ashr_i32 s7, s7, 31
	v_readfirstlane_b32 s20, v1
	s_mul_i32 s6, s6, s20
	s_mul_hi_u32 s6, s20, s6
	s_add_i32 s20, s20, s6
	s_mul_hi_u32 s6, s1, s20
	s_mul_i32 s20, s6, s0
	s_sub_i32 s1, s1, s20
	s_add_i32 s20, s6, 1
	s_sub_i32 s21, s1, s0
	s_cmp_ge_u32 s1, s0
	s_cselect_b32 s6, s20, s6
	s_cselect_b32 s1, s21, s1
	s_add_i32 s20, s6, 1
	s_cmp_ge_u32 s1, s0
	s_cselect_b32 s0, s20, s6
	s_abs_i32 s6, s90
	v_cvt_f32_u32_e32 v1, s6
	s_sub_i32 s20, 0, s6
	s_xor_b32 s0, s0, s7
	s_sub_i32 s69, s0, s7
	v_rcp_iflag_f32_e32 v1, v1
	s_add_i32 s0, s90, 0x2fff
	s_xor_b32 s7, s0, s90
	s_abs_i32 s0, s0
	v_mul_f32_e32 v1, 0x4f7ffffe, v1
	v_cvt_u32_f32_e32 v1, v1
	s_ashr_i32 s7, s7, 31
	v_lshlrev_b32_e32 v4, 1, v159
	v_lshrrev_b32_e32 v3, 2, v159
	v_readfirstlane_b32 s21, v1
	s_mul_i32 s20, s20, s21
	s_mul_hi_u32 s20, s21, s20
	s_add_i32 s21, s21, s20
	s_mul_hi_u32 s20, s0, s21
	s_mul_i32 s21, s20, s6
	s_sub_i32 s0, s0, s21
	s_add_i32 s21, s20, 1
	s_sub_i32 s22, s0, s6
	s_cmp_ge_u32 s0, s6
	s_cselect_b32 s20, s21, s20
	s_cselect_b32 s0, s22, s0
	s_add_i32 s21, s20, 1
	s_cmp_ge_u32 s0, s6
	s_cselect_b32 s0, s21, s20
	s_max_i32 s6, s69, 1
	v_cvt_f32_u32_e32 v1, s6
	s_xor_b32 s0, s0, s7
	s_sub_i32 s0, s0, s7
	s_mul_i32 s7, s0, s34
	v_rcp_iflag_f32_e32 v1, v1
	v_and_b32_e32 v4, 32, v4
	s_add_i32 s67, s7, 0x7800
	s_sub_i32 s20, 0, s6
	v_mul_f32_e32 v1, 0x4f7ffffe, v1
	v_cvt_u32_f32_e32 v1, v1
	s_add_i32 s7, s67, s0
	s_add_i32 s0, s6, s0
	s_add_i32 s0, s0, -1
	v_readfirstlane_b32 s21, v1
	v_lshlrev_b32_e32 v1, 3, v159
	v_and_b32_e32 v2, 0x1c0, v1
	v_add_u32_e32 v163, s68, v2
	v_and_b32_e32 v165, 56, v1
	v_bfe_u32 v2, v0, 2, 2
	v_and_b32_e32 v1, 24, v1
	v_add3_u32 v167, s68, v4, v1
	v_and_or_b32 v1, v3, 8, v2
	s_mul_i32 s20, s20, s21
	v_lshlrev_b32_e32 v169, 6, v1
	v_lshlrev_b32_e32 v1, 8, v159
	s_mul_hi_u32 s20, s21, s20
	v_and_b32_e32 v1, 0x1f00, v1
	v_lshrrev_b32_e32 v2, 5, v159
	s_min_i32 s66, s7, 0xa800
	s_ashr_i32 s7, s0, 31
	s_abs_i32 s0, s0
	s_add_i32 s21, s21, s20
	v_add_u32_e32 v204, s68, v1
	v_and_b32_e32 v1, 15, v0
	v_bitop3_b32 v3, v2, v0, 15 bitop3:0x78
	s_mul_hi_u32 s20, s0, s21
	v_lshlrev_b32_e32 v205, 4, v3
	v_bitop3_b32 v3, v2, v1, 2 bitop3:0x36
	s_mul_i32 s21, s20, s6
	v_lshlrev_b32_e32 v206, 4, v3
	v_bitop3_b32 v3, v2, v1, 4 bitop3:0x36
	s_sub_i32 s0, s0, s21
	v_lshlrev_b32_e32 v207, 4, v3
	v_bitop3_b32 v3, v2, v1, 6 bitop3:0x36
	s_add_i32 s21, s20, 1
	s_sub_i32 s22, s0, s6
	v_lshlrev_b32_e32 v208, 4, v3
	v_bitop3_b32 v3, v2, v1, 8 bitop3:0x36
	s_cmp_ge_u32 s0, s6
	v_lshlrev_b32_e32 v209, 4, v3
	v_bitop3_b32 v3, v2, v1, 10 bitop3:0x36
	s_cselect_b32 s20, s21, s20
	v_lshlrev_b32_e32 v210, 4, v3
	v_bitop3_b32 v3, v2, v1, 12 bitop3:0x36
	v_bitop3_b32 v1, v2, v1, 14 bitop3:0x36
	v_and_b32_e32 v0, 7, v0
	s_cselect_b32 s0, s22, s0
	s_add_i32 s21, s20, 1
	v_lshrrev_b32_e32 v158, 3, v159
	v_lshlrev_b32_e32 v212, 4, v1
	v_lshlrev_b32_e32 v1, 1, v0
	s_cmp_ge_u32 s0, s6
	v_lshlrev_b32_e32 v160, 4, v0
	v_xor_b32_e32 v0, v158, v1
	s_cselect_b32 s0, s21, s20
	v_lshlrev_b32_e32 v214, 4, v0
	v_bitop3_b32 v0, v1, v158, 1 bitop3:0x36
	s_xor_b32 s0, s0, s7
	v_or_b32_e32 v2, 1, v1
	v_lshlrev_b32_e32 v215, 4, v0
	v_bitop3_b32 v0, v158, v1, 8 bitop3:0x36
	s_sub_i32 s72, s0, s7
	s_add_i32 s72, s72, 1
	s_and_b32 s72, s72, -2
	s_lshl_b32 s73, s6, 1
	v_lshlrev_b32_e32 v217, 4, v0
	v_bitop3_b32 v0, v158, v2, 8 bitop3:0x36
	v_or_b32_e32 v166, 24, v158
	s_cmpk_gt_u32 s74, 0xff
	v_lshlrev_b32_e32 v218, 4, v0
	v_bitop3_b32 v0, v166, v1, 15 bitop3:0x6c
	v_mov_b32_e32 v171, 0
	v_or_b32_e32 v162, 8, v158
	v_or_b32_e32 v164, 16, v158
	v_lshlrev_b32_e32 v221, 4, v0
	v_bitop3_b32 v0, v166, v2, 15 bitop3:0x6c
	s_cselect_b64 s[6:7], -1, 0
	s_mov_b32 s20, 0x3f803f80
	s_mov_b32 s1, 0
	s_mov_b32 s96, s74
	v_and_b32_e32 v168, 28, v157
	v_lshlrev_b32_e32 v211, 4, v3
	v_mov_b32_e32 v161, v171
	v_lshl_add_u32 v213, v158, 8, s68
	v_lshl_add_u32 v216, v162, 8, s68
	v_lshl_add_u32 v219, v164, 8, s68
	v_lshl_add_u32 v220, v166, 8, s68
	v_lshlrev_b32_e32 v222, 4, v0
	v_cndmask_b32_e64 v223, 0, 1, s[6:7]
	s_movk_i32 s74, 0x60
	s_add_i32 s75, 0, 0x180b4
	s_mov_b32 s76, 0x5fc0000
	s_mov_b32 s77, 0x6fc0000
	s_mov_b32 s78, 0x5fd0000
	s_mov_b32 s79, 0x6fd0000
	s_mov_b32 s80, 0x5fe0000
	s_mov_b32 s81, 0x6fe0000
	s_mov_b32 s40, 0x3f803f80
	s_mov_b32 s41, s20
	s_mov_b32 s42, s20
	s_mov_b32 s43, s20
	v_mov_b32_e32 v0, 0x3f803f80
	s_mov_b32 s82, 0
	s_mov_b32 s83, 0
	s_waitcnt lgkmcnt(0)
	s_barrier
	s_branch .LBB0_214
